# end of U phase: the wave's 18 one-KiB pieces of the V channel slice are loaded back to back and written to LDS on a vmcnt ladder instead of load-wait-write one at a time
# speedup vs baseline: 1.0051x; 1.0001x over previous
; __device__ __forceinline__ int mk_lane() { int l_ = (int)__builtin_amdgcn_mbcnt_hi(~0u, __builtin_amdgcn_mbcnt_lo(~0u, 0u)); asm volatile("" : "+v"(l_)); return l_; }
; #define GAS __attribute__((address_space(1)))
; #define LAS __attribute__((address_space(3)))
; __device__ __forceinline__ void xcd_barrier(const XcdBarrier& b, int wave_id, int pair = -1) {
;     asm volatile("s_waitcnt vmcnt(0)" ::: "memory");
;     __syncthreads();
;     if (wave_id == 0 && mk_lane() == 0) {
;         unsigned* bar = b.bar;
;         __builtin_amdgcn_s_waitcnt(0);
;         unsigned nloc = b.st[0], nx = b.st[1];
;         if (nloc == 0u) { xcd_barrier_complete(bar, b.x, nloc, nx); b.st[0] = nloc; b.st[1] = nx; }
; template <int VAR> __device__ __forceinline__ void peer_u_phase(int wave, int grp, int gwl  , LAS unsigned char* lds, gu32* qhead  , const unsigned char* __restrict__ X1Q, const unsigned char* __restrict__ UT, ...
;     ...
;     if (VS_next != nullptr) {
;         const int lo = wave * (U_WAVE_LDS / 16) + lane, hi = (wave + 1) * (U_WAVE_LDS / 16) < 8192 ? (wave + 1) * (U_WAVE_LDS / 16) : 8192;
;         const GAS v4u* src = (const GAS v4u*)VS_next;
; #pragma unroll
;         for (int k = 0; k < U_WAVE_LDS / 1024; ++k) { const int i = lo + 64 * k; if (i < hi) *(LAS v4u*)(lds + i * 16) = src[i]; }
;     }
.LBB0_859:
	s_lshl_b32 s3, s23, 17
	s_and_b32 s3, s3, 0xfe0000
	s_add_u32 s3, s8, s3
	s_addc_u32 s5, s9, 0
	s_add_u32 s4, s3, 0x17000000
	s_mul_i32 s3, s61, 0x480
	s_addc_u32 s5, s5, 0
	v_add_u32_e32 v0, s3, v136
	s_addk_i32 s3, 0x480
	s_min_i32 s3, s3, 0x2000
	v_cmp_gt_i32_e32 vcc, s3, v0
	v_ashrrev_i32_e32 v1, 31, v0
	s_mov_b64 s[6:7], exec
	v_ashrrev_i32_e32 v1, 31, v0
	v_lshl_add_u64 v[2:3], v[0:1], 4, s[4:5]
	v_lshlrev_b32_e32 v6, 4, v0
	s_mov_b64 s[10:11], 0x1000
	global_load_dwordx4 v[8:11], v[2:3], off
	global_load_dwordx4 v[12:15], v[2:3], off offset:1024
	s_cmp_eq_u32 s61, 7
	s_cbranch_scc1 .Lvfill7_0
	global_load_dwordx4 v[16:19], v[2:3], off offset:2048
	global_load_dwordx4 v[20:23], v[2:3], off offset:3072
	v_lshl_add_u64 v[4:5], v[2:3], 0, s[10:11]
	global_load_dwordx4 v[24:27], v[4:5], off
	global_load_dwordx4 v[28:31], v[4:5], off offset:1024
	global_load_dwordx4 v[32:35], v[4:5], off offset:2048
	global_load_dwordx4 v[36:39], v[4:5], off offset:3072
	v_lshl_add_u64 v[2:3], v[4:5], 0, s[10:11]
	global_load_dwordx4 v[40:43], v[2:3], off
	global_load_dwordx4 v[44:47], v[2:3], off offset:1024
	global_load_dwordx4 v[48:51], v[2:3], off offset:2048
	global_load_dwordx4 v[52:55], v[2:3], off offset:3072
	v_lshl_add_u64 v[4:5], v[2:3], 0, s[10:11]
	global_load_dwordx4 v[56:59], v[4:5], off
	global_load_dwordx4 v[60:63], v[4:5], off offset:1024
	global_load_dwordx4 v[64:67], v[4:5], off offset:2048
	global_load_dwordx4 v[68:71], v[4:5], off offset:3072
	v_lshl_add_u64 v[2:3], v[4:5], 0, s[10:11]
	global_load_dwordx4 v[72:75], v[2:3], off
	global_load_dwordx4 v[76:79], v[2:3], off offset:1024
	s_waitcnt vmcnt(17)
	ds_write_b128 v6, v[8:11]
	s_waitcnt vmcnt(16)
	ds_write_b128 v6, v[12:15] offset:1024
	s_waitcnt vmcnt(15)
	ds_write_b128 v6, v[16:19] offset:2048
	s_waitcnt vmcnt(14)
	ds_write_b128 v6, v[20:23] offset:3072
	s_waitcnt vmcnt(13)
	ds_write_b128 v6, v[24:27] offset:4096
	s_waitcnt vmcnt(12)
	ds_write_b128 v6, v[28:31] offset:5120
	s_waitcnt vmcnt(11)
	ds_write_b128 v6, v[32:35] offset:6144
	s_waitcnt vmcnt(10)
	ds_write_b128 v6, v[36:39] offset:7168
	s_waitcnt vmcnt(9)
	ds_write_b128 v6, v[40:43] offset:8192
	s_waitcnt vmcnt(8)
	ds_write_b128 v6, v[44:47] offset:9216
	s_waitcnt vmcnt(7)
	ds_write_b128 v6, v[48:51] offset:10240
	s_waitcnt vmcnt(6)
	ds_write_b128 v6, v[52:55] offset:11264
	s_waitcnt vmcnt(5)
	ds_write_b128 v6, v[56:59] offset:12288
	s_waitcnt vmcnt(4)
	ds_write_b128 v6, v[60:63] offset:13312
	s_waitcnt vmcnt(3)
	ds_write_b128 v6, v[64:67] offset:14336
	s_waitcnt vmcnt(2)
	ds_write_b128 v6, v[68:71] offset:15360
	s_waitcnt vmcnt(1)
	ds_write_b128 v6, v[72:75] offset:16384
	s_waitcnt vmcnt(0)
	ds_write_b128 v6, v[76:79] offset:17408
	s_branch .Lvfilld_0
.Lvfill7_0:
	s_waitcnt vmcnt(1)
	ds_write_b128 v6, v[8:11]
	s_waitcnt vmcnt(0)
	ds_write_b128 v6, v[12:15] offset:1024
.Lvfilld_0:
	s_cmp_lt_i32 s41, 7
	s_cbranch_scc1 .LBB0_951
	s_waitcnt vmcnt(0)
	s_andn2_b64 vcc, exec, s[38:39]
	s_waitcnt lgkmcnt(0)
	s_barrier
	s_cbranch_vccnz .LBB0_950
	s_nop 0
	v_cmp_eq_u32_e32 vcc, 0, v177
	s_and_saveexec_b64 s[4:5], vcc
	s_cbranch_execz .LBB0_949
	s_add_i32 s3, 0, 0x27f60
	v_mov_b32_e32 v0, s3
	s_waitcnt vmcnt(0) expcnt(0) lgkmcnt(0)
	ds_read_b32 v2, v0
	s_add_i32 s3, 0, 0x27f64
	v_mov_b32_e32 v0, s3
	ds_read_b32 v0, v0
	s_waitcnt lgkmcnt(1)
	v_cmp_ne_u32_e32 vcc, 0, v2
	s_cbranch_vccnz .LBB0_913
	v_readlane_b32 s6, v248, 0
	v_readlane_b32 s7, v248, 1
	s_load_dwordx2 s[10:11], s[6:7], 0x4
	s_add_u32 s6, s30, 0x4200
	s_addc_u32 s7, s31, 0
	s_add_u32 s8, s30, 0x4400
	s_addc_u32 s9, s31, 0
	s_waitcnt lgkmcnt(0)
	s_mul_i32 s3, s10, s60
	s_add_u32 s10, s30, 0x4500
	s_mul_i32 s3, s3, s11
	s_addc_u32 s11, s31, 0
	s_add_u32 s12, s30, 0x4600
	s_addc_u32 s13, s31, 0
	s_add_u32 s14, s30, 0x4700
	s_addc_u32 s15, s31, 0
	s_add_u32 s16, s30, 0x4800
	s_addc_u32 s17, s31, 0
	s_add_u32 s18, s30, 0x4900
	s_addc_u32 s19, s31, 0
	s_add_u32 s20, s30, 0x4a00
	s_addc_u32 s21, s31, 0
	s_add_u32 s22, s30, 0x4b00
	s_addc_u32 s23, s31, 0
	s_add_u32 s24, s30, 0x4c00
	s_addc_u32 s25, s31, 0
	s_add_u32 s26, s30, 0x4d00
	s_addc_u32 s27, s31, 0
	s_add_u32 s28, s30, 0x4e00
	s_addc_u32 s29, s31, 0
	s_add_u32 s42, s30, 0x4f00
	s_addc_u32 s43, s31, 0
	s_add_u32 s44, s30, 0x5000
	s_addc_u32 s45, s31, 0
	s_add_u32 s46, s30, 0x5100
	s_addc_u32 s47, s31, 0
	s_add_u32 s48, s30, 0x5200
	s_addc_u32 s49, s31, 0
	s_add_u32 s50, s30, 0x5300
	s_addc_u32 s51, s31, 0
	s_mov_b32 s58, 1
	v_mov_b32_e32 v16, 0
	s_branch .LBB0_901

; #define GAS __attribute__((address_space(1)))
; #define LAS __attribute__((address_space(3)))
; template <int VAR> __device__ __forceinline__ void peer_u_phase(int wave, int grp, int gwl  , LAS unsigned char* lds, gu32* qhead  , const unsigned char* __restrict__ X1Q, const unsigned char* __restrict__ UT, ...
;     ...
;     if (VS_next != nullptr) {
;         const int lo = wave * (U_WAVE_LDS / 16) + lane, hi = (wave + 1) * (U_WAVE_LDS / 16) < 8192 ? (wave + 1) * (U_WAVE_LDS / 16) : 8192;
;         const GAS v4u* src = (const GAS v4u*)VS_next;
; #pragma unroll
;         for (int k = 0; k < U_WAVE_LDS / 1024; ++k) { const int i = lo + 64 * k; if (i < hi) *(LAS v4u*)(lds + i * 16) = src[i]; }
;     }
.LBB0_1855:
	s_lshl_b32 s3, s23, 17
	s_and_b32 s3, s3, 0xfe0000
	s_add_u32 s3, s8, s3
	s_addc_u32 s5, s9, 0
	s_add_u32 s4, s3, 0x18000000
	s_mul_i32 s3, s61, 0x480
	s_addc_u32 s5, s5, 0
	v_add_u32_e32 v0, s3, v136
	s_addk_i32 s3, 0x480
	s_min_i32 s3, s3, 0x2000
	v_cmp_gt_i32_e32 vcc, s3, v0
	s_mov_b64 s[6:7], exec
	v_ashrrev_i32_e32 v1, 31, v0
	v_lshl_add_u64 v[2:3], v[0:1], 4, s[4:5]
	v_lshlrev_b32_e32 v6, 4, v0
	s_mov_b64 s[10:11], 0x1000
	global_load_dwordx4 v[8:11], v[2:3], off
	global_load_dwordx4 v[12:15], v[2:3], off offset:1024
	s_cmp_eq_u32 s61, 7
	s_cbranch_scc1 .Lvfill7_1
	global_load_dwordx4 v[16:19], v[2:3], off offset:2048
	global_load_dwordx4 v[20:23], v[2:3], off offset:3072
	v_lshl_add_u64 v[4:5], v[2:3], 0, s[10:11]
	global_load_dwordx4 v[24:27], v[4:5], off
	global_load_dwordx4 v[28:31], v[4:5], off offset:1024
	global_load_dwordx4 v[32:35], v[4:5], off offset:2048
	global_load_dwordx4 v[36:39], v[4:5], off offset:3072
	v_lshl_add_u64 v[2:3], v[4:5], 0, s[10:11]
	global_load_dwordx4 v[40:43], v[2:3], off
	global_load_dwordx4 v[44:47], v[2:3], off offset:1024
	global_load_dwordx4 v[48:51], v[2:3], off offset:2048
	global_load_dwordx4 v[52:55], v[2:3], off offset:3072
	v_lshl_add_u64 v[4:5], v[2:3], 0, s[10:11]
	global_load_dwordx4 v[56:59], v[4:5], off
	global_load_dwordx4 v[60:63], v[4:5], off offset:1024
	global_load_dwordx4 v[64:67], v[4:5], off offset:2048
	global_load_dwordx4 v[68:71], v[4:5], off offset:3072
	v_lshl_add_u64 v[2:3], v[4:5], 0, s[10:11]
	global_load_dwordx4 v[72:75], v[2:3], off
	global_load_dwordx4 v[76:79], v[2:3], off offset:1024
	s_waitcnt vmcnt(17)
	ds_write_b128 v6, v[8:11]
	s_waitcnt vmcnt(16)
	ds_write_b128 v6, v[12:15] offset:1024
	s_waitcnt vmcnt(15)
	ds_write_b128 v6, v[16:19] offset:2048
	s_waitcnt vmcnt(14)
	ds_write_b128 v6, v[20:23] offset:3072
	s_waitcnt vmcnt(13)
	ds_write_b128 v6, v[24:27] offset:4096
	s_waitcnt vmcnt(12)
	ds_write_b128 v6, v[28:31] offset:5120
	s_waitcnt vmcnt(11)
	ds_write_b128 v6, v[32:35] offset:6144
	s_waitcnt vmcnt(10)
	ds_write_b128 v6, v[36:39] offset:7168
	s_waitcnt vmcnt(9)
	ds_write_b128 v6, v[40:43] offset:8192
	s_waitcnt vmcnt(8)
	ds_write_b128 v6, v[44:47] offset:9216
	s_waitcnt vmcnt(7)
	ds_write_b128 v6, v[48:51] offset:10240
	s_waitcnt vmcnt(6)
	ds_write_b128 v6, v[52:55] offset:11264
	s_waitcnt vmcnt(5)
	ds_write_b128 v6, v[56:59] offset:12288
	s_waitcnt vmcnt(4)
	ds_write_b128 v6, v[60:63] offset:13312
	s_waitcnt vmcnt(3)
	ds_write_b128 v6, v[64:67] offset:14336
	s_waitcnt vmcnt(2)
	ds_write_b128 v6, v[68:71] offset:15360
	s_waitcnt vmcnt(1)
	ds_write_b128 v6, v[72:75] offset:16384
	s_waitcnt vmcnt(0)
	ds_write_b128 v6, v[76:79] offset:17408
	s_branch .Lvfilld_1

; __device__ __forceinline__ int mk_lane() { int l_ = (int)__builtin_amdgcn_mbcnt_hi(~0u, __builtin_amdgcn_mbcnt_lo(~0u, 0u)); asm volatile("" : "+v"(l_)); return l_; }
; #define GAS __attribute__((address_space(1)))
; #define LAS __attribute__((address_space(3)))
; __device__ __forceinline__ void xcd_barrier(const XcdBarrier& b, int wave_id, int pair = -1) {
;     asm volatile("s_waitcnt vmcnt(0)" ::: "memory");
;     __syncthreads();
;     if (wave_id == 0 && mk_lane() == 0) {
;         unsigned* bar = b.bar;
;         __builtin_amdgcn_s_waitcnt(0);
;         unsigned nloc = b.st[0], nx = b.st[1];
;         if (nloc == 0u) { xcd_barrier_complete(bar, b.x, nloc, nx); b.st[0] = nloc; b.st[1] = nx; }
; template <int VAR> __device__ __forceinline__ void peer_u_phase(int wave, int grp, int gwl  , LAS unsigned char* lds, gu32* qhead  , const unsigned char* __restrict__ X1Q, const unsigned char* __restrict__ UT, ...
;     ...
;     if (VS_next != nullptr) {
;         const int lo = wave * (U_WAVE_LDS / 16) + lane, hi = (wave + 1) * (U_WAVE_LDS / 16) < 8192 ? (wave + 1) * (U_WAVE_LDS / 16) : 8192;
;         const GAS v4u* src = (const GAS v4u*)VS_next;
; #pragma unroll
;         for (int k = 0; k < U_WAVE_LDS / 1024; ++k) { const int i = lo + 64 * k; if (i < hi) *(LAS v4u*)(lds + i * 16) = src[i]; }
;     }
.Lvfilld_1:
	s_cmp_lt_i32 s41, 14
	s_cbranch_scc1 .LBB0_1947
	s_waitcnt vmcnt(0)
	s_andn2_b64 vcc, exec, s[38:39]
	s_waitcnt lgkmcnt(0)
	s_barrier
	s_cbranch_vccnz .LBB0_1946
	s_nop 0
	v_cmp_eq_u32_e32 vcc, 0, v177
	s_and_saveexec_b64 s[4:5], vcc
	s_cbranch_execz .LBB0_1945
	s_add_i32 s3, 0, 0x27f60
	v_mov_b32_e32 v0, s3
	s_waitcnt vmcnt(0) expcnt(0) lgkmcnt(0)
	ds_read_b32 v2, v0
	s_add_i32 s3, 0, 0x27f64
	v_mov_b32_e32 v0, s3
	ds_read_b32 v0, v0
	s_waitcnt lgkmcnt(1)
	v_cmp_ne_u32_e32 vcc, 0, v2
	s_cbranch_vccnz .LBB0_1909
	v_readlane_b32 s6, v248, 0
	v_readlane_b32 s7, v248, 1
	s_load_dwordx2 s[10:11], s[6:7], 0x4
	s_add_u32 s6, s30, 0x4200
	s_addc_u32 s7, s31, 0
	s_add_u32 s8, s30, 0x4400
	s_addc_u32 s9, s31, 0
	s_waitcnt lgkmcnt(0)
	s_mul_i32 s3, s10, s60
	s_add_u32 s10, s30, 0x4500
	s_mul_i32 s3, s3, s11
	s_addc_u32 s11, s31, 0
	s_add_u32 s12, s30, 0x4600
	s_addc_u32 s13, s31, 0
	s_add_u32 s14, s30, 0x4700
	s_addc_u32 s15, s31, 0
	s_add_u32 s16, s30, 0x4800
	s_addc_u32 s17, s31, 0
	s_add_u32 s18, s30, 0x4900
	s_addc_u32 s19, s31, 0
	s_add_u32 s20, s30, 0x4a00
	s_addc_u32 s21, s31, 0
	s_add_u32 s22, s30, 0x4b00
	s_addc_u32 s23, s31, 0
	s_add_u32 s24, s30, 0x4c00
	s_addc_u32 s25, s31, 0
	s_add_u32 s26, s30, 0x4d00
	s_addc_u32 s27, s31, 0
	s_add_u32 s28, s30, 0x4e00
	s_addc_u32 s29, s31, 0
	s_add_u32 s42, s30, 0x4f00
	s_addc_u32 s43, s31, 0
	s_add_u32 s44, s30, 0x5000
	s_addc_u32 s45, s31, 0
	s_add_u32 s46, s30, 0x5100
	s_addc_u32 s47, s31, 0
	s_add_u32 s48, s30, 0x5200
	s_addc_u32 s49, s31, 0
	s_add_u32 s50, s30, 0x5300
	s_addc_u32 s51, s31, 0
	s_mov_b32 s58, 1
	v_mov_b32_e32 v16, 0
	s_branch .LBB0_1897
